# P0 expert-weight conversion: gain loads hoisted before the next item's prefetch so the prefetch stays in flight (counted vmcnt)
# speedup vs baseline: 1.0187x; 1.0008x over previous
; #define GAS __attribute__((address_space(1)))
; #define LAS __attribute__((address_space(3)))
; __device__ __forceinline__ void tr8_load(TrRegs& R, const TrP& p, int lane) {
;     const int nq = (lane & 7) * 4, kr = lane >> 3;
; #pragma unroll
;     for (int i = 0; i < 8; ++i) R.v[i] = __builtin_nontemporal_load((const GAS f32x4*)(p.W + (size_t)(p.k0 + 8 * i + kr) * p.ldw + p.n0 + nq));
; }
; __device__ __forceinline__ void moe_weight_items(Frame& F, int layer, int gw, int NGW) {
;     LAS float* scr = (LAS float*)(F.lds + RING_OFF + F.wave * 16384);
;     unsigned char* WGU = F.ws + WS_WGU; unsigned char* WD = F.ws + WS_WD;
;     if (gw >= MOE_ITEMS) return;
;     TrP pc = moe_item_params(layer, gw, WGU, WD); TrRegs rc; tr8_load(rc, pc, F.lane);
;     for (int it = gw; it < MOE_ITEMS; it += NGW) {
;         const int nx = it + NGW; TrP pn = pc; TrRegs rn;
;         if (nx < MOE_ITEMS) { pn = moe_item_params(layer, nx, WGU, WD); tr8_load(rn, pn, F.lane); }
.LBB0_101:
	v_lshrrev_b32_e32 v66, 3, v75
	v_add_u32_e32 v1, s12, v66
	v_add_u32_e32 v2, 56, v1
	v_mad_i64_i32 v[2:3], s[38:39], s24, v2, 0
	s_ashr_i32 s23, s22, 31
	v_lshlrev_b32_e32 v4, 2, v0
	v_lshl_add_u64 v[2:3], v[2:3], 2, s[2:3]
	s_lshl_b64 s[22:23], s[22:23], 2
	v_and_b32_e32 v10, 28, v4
	v_lshl_add_u64 v[2:3], v[2:3], 0, s[22:23]
	v_mov_b32_e32 v69, 0
	v_lshlrev_b32_e32 v68, 2, v10
	v_lshl_add_u64 v[12:13], v[2:3], 0, v[68:69]
	v_add_u32_e32 v2, 48, v1
	v_mad_i64_i32 v[2:3], s[38:39], s24, v2, 0
	v_lshl_add_u64 v[2:3], v[2:3], 2, s[2:3]
	v_lshl_add_u64 v[2:3], v[2:3], 0, s[22:23]
	v_add_u32_e32 v11, 40, v1
	v_lshl_add_u64 v[14:15], v[2:3], 0, v[68:69]
	global_load_dwordx4 v[2:5], v[12:13], off nt
	global_load_dwordx4 v[6:9], v[14:15], off nt
	v_mad_i64_i32 v[12:13], s[38:39], s24, v11, 0
	v_add_u32_e32 v11, 32, v1
	v_lshl_add_u64 v[12:13], v[12:13], 2, s[2:3]
	v_mad_i64_i32 v[14:15], s[38:39], s24, v11, 0
	v_lshl_add_u64 v[12:13], v[12:13], 0, s[22:23]
	v_lshl_add_u64 v[14:15], v[14:15], 2, s[2:3]
	v_lshl_add_u64 v[12:13], v[12:13], 0, v[68:69]
	v_lshl_add_u64 v[14:15], v[14:15], 0, s[22:23]
	v_add_u32_e32 v11, 24, v1
	v_lshl_add_u64 v[14:15], v[14:15], 0, v[68:69]
	global_load_dwordx4 v[18:21], v[12:13], off nt
	global_load_dwordx4 v[26:29], v[14:15], off nt
	v_mad_i64_i32 v[12:13], s[38:39], s24, v11, 0
	v_add_u32_e32 v11, 16, v1
	v_lshl_add_u64 v[12:13], v[12:13], 2, s[2:3]
	v_mad_i64_i32 v[14:15], s[38:39], s24, v11, 0
	v_lshl_add_u64 v[12:13], v[12:13], 0, s[22:23]
	v_lshl_add_u64 v[14:15], v[14:15], 2, s[2:3]
	v_lshl_add_u64 v[12:13], v[12:13], 0, v[68:69]
	v_lshl_add_u64 v[14:15], v[14:15], 0, s[22:23]
	v_add_u32_e32 v11, 8, v1
	v_lshl_add_u64 v[14:15], v[14:15], 0, v[68:69]
	global_load_dwordx4 v[50:53], v[12:13], off nt
	global_load_dwordx4 v[54:57], v[14:15], off nt
	v_mad_i64_i32 v[12:13], s[38:39], s24, v11, 0
	v_lshl_add_u64 v[12:13], v[12:13], 2, s[2:3]
	v_mad_i64_i32 v[14:15], s[24:25], s24, v1, 0
	v_lshl_add_u64 v[12:13], v[12:13], 0, s[22:23]
	v_lshl_add_u64 v[14:15], v[14:15], 2, s[2:3]
	v_lshl_add_u64 v[12:13], v[12:13], 0, v[68:69]
	v_lshl_add_u64 v[14:15], v[14:15], 0, s[22:23]
	v_lshl_add_u64 v[14:15], v[14:15], 0, v[68:69]
	global_load_dwordx4 v[58:61], v[12:13], off nt
	global_load_dwordx4 v[62:65], v[14:15], off nt
	v_and_b32_e32 v11, 7, v0
	v_lshl_add_u32 v12, v11, 4, s7
	v_mul_u32_u24_e32 v13, 0x84, v66
	v_lshlrev_b32_e32 v70, 3, v11
	v_mul_u32_u24_e32 v11, 0x420, v11
	v_lshlrev_b32_e32 v14, 2, v66
	s_add_i32 s2, s8, s6
	v_or_b32_e32 v1, 8, v66
	v_or_b32_e32 v76, 16, v66
	v_or_b32_e32 v77, 24, v66
	v_mov_b32_e32 v71, v69
	v_add3_u32 v78, s7, v11, v14
	v_mov_b32_e32 v67, v69
	s_lshl_b32 s7, s2, 5
	s_lshl_b32 s44, s8, 5
	s_movk_i32 s45, 0xb8
	v_lshlrev_b32_e32 v68, 2, v10
	v_add_u32_e32 v79, v12, v13
	s_mov_b32 s46, s6
	s_mov_b64 s[38:39], s[18:19]
	s_mov_b64 s[22:23], s[14:15]
	s_mov_b32 s47, s17
	s_mov_b32 s48, s37
	s_waitcnt vmcnt(0)
	s_branch .LBB0_104

; #define GAS __attribute__((address_space(1)))
; #define LAS __attribute__((address_space(3)))
; #define LDS_WAIT() asm volatile("s_waitcnt lgkmcnt(0)" ::: "memory")
; __device__ __forceinline__ unsigned pk4_fp8(float a, float b, float c, float d) { unsigned w = 0u; w = __builtin_amdgcn_cvt_pk_fp8_f32(a, b, w, false); w = __builtin_amdgcn_cvt_pk_fp8_f32(c, d, w, true); return w; }
; __device__ __forceinline__ void tr8_finish(const TrRegs& R, const TrP& p, LAS float* scr, int lane) {
;     const int nq = (lane & 7) * 4, kr = lane >> 3;
; #pragma unroll
;     for (int i = 0; i < 8; ++i) { const int kk = 8 * i + kr; float gs = p.scale; if (p.gain) gs *= p.gain[p.k0 + kk];
;         LAS float* d = scr + kk * 33 + nq; d[0] = R.v[i][0] * gs; d[1] = R.v[i][1] * gs; d[2] = R.v[i][2] * gs; d[3] = R.v[i][3] * gs; }
;     LDS_WAIT(); asm volatile("" ::: "memory");
;     const int c = lane & 7;
; #pragma unroll
;     for (int j = 0; j < 4; ++j) { const int n = (lane >> 3) + 8 * j; const LAS float* s = scr + (8 * c) * 33 + n;
;         u32x2 o; o.x = pk4_fp8(s[0 * 33], s[1 * 33], s[2 * 33], s[3 * 33]); o.y = pk4_fp8(s[4 * 33], s[5 * 33], s[6 * 33], s[7 * 33]);
;         *(GAS u32x2*)(p.D + (size_t)(p.drow0 + n) * p.ldd + p.k0 + 8 * c) = o; }
;     LDS_WAIT(); asm volatile("" ::: "memory");
; }
; __device__ __forceinline__ void moe_weight_items(Frame& F, int layer, int gw, int NGW) {
;     LAS float* scr = (LAS float*)(F.lds + RING_OFF + F.wave * 16384);
;     unsigned char* WGU = F.ws + WS_WGU; unsigned char* WD = F.ws + WS_WD;
;     if (gw >= MOE_ITEMS) return;
;     TrP pc = moe_item_params(layer, gw, WGU, WD); TrRegs rc; tr8_load(rc, pc, F.lane);
;     for (int it = gw; it < MOE_ITEMS; it += NGW) {
;         const int nx = it + NGW; TrP pn = pc; TrRegs rn;
;         if (nx < MOE_ITEMS) { pn = moe_item_params(layer, nx, WGU, WD); tr8_load(rn, pn, F.lane); }
;         tr8_finish(rc, pc, scr, F.lane);
;         if (nx < MOE_ITEMS) { pc = pn; rc = rn; }
;     }
.LBB0_103:
	v_mov_b32_e32 v19, v20
	v_pk_mul_f32 v[2:3], v[2:3], v[18:19]
	v_add_u32_e32 v6, 0x1ce0, v79
	ds_write2_b32 v6, v2, v3 offset1:1
	v_pk_mul_f32 v[2:3], v[4:5], v[18:19]
	v_add_u32_e32 v4, 0x1ce8, v79
	ds_write2_b32 v4, v2, v3 offset1:1
	s_waitcnt lgkmcnt(0)
	ds_read2_b32 v[2:3], v78 offset0:33 offset1:41
	ds_read2_b32 v[4:5], v78 offset0:66 offset1:74
	ds_read2_b32 v[6:7], v78 offset1:8
	ds_read2_b32 v[8:9], v78 offset0:99 offset1:107
	ds_read2_b32 v[20:21], v78 offset0:132 offset1:140
	ds_read2_b32 v[26:27], v78 offset0:165 offset1:173
	v_mov_b32_e32 v18, 0
	ds_read2_b32 v[28:29], v78 offset0:198 offset1:206
	ds_read2_b32 v[50:51], v78 offset0:231 offset1:239
	s_waitcnt lgkmcnt(5)
	v_cvt_pk_fp8_f32 v18, v6, v2
	v_mov_b32_e32 v19, 0
	s_waitcnt lgkmcnt(2)
	v_cvt_pk_fp8_f32 v19, v20, v26
	v_add_u32_e32 v2, s37, v66
	v_mov_b64_e32 v[52:53], s[14:15]
	v_mad_u64_u32 v[54:55], s[2:3], v2, s17, v[52:53]
	v_cvt_pk_fp8_f32 v18, v4, v8 op_sel:[0,0,1]
	v_ashrrev_i32_e32 v4, 31, v2
	v_mov_b32_e32 v2, v55
	v_mad_u64_u32 v[56:57], s[2:3], v4, s17, v[2:3]
	v_mov_b32_e32 v2, 0
	s_waitcnt lgkmcnt(0)
	v_cvt_pk_fp8_f32 v19, v28, v50 op_sel:[0,0,1]
	v_cvt_pk_fp8_f32 v2, v7, v3
	v_mov_b32_e32 v55, v56
	v_lshl_add_u64 v[54:55], v[54:55], 0, s[12:13]
	v_mov_b32_e32 v3, 0
	v_cvt_pk_fp8_f32 v3, v21, v27
	v_lshl_add_u64 v[6:7], v[54:55], 0, v[70:71]
	v_add_u32_e32 v4, s37, v1
	global_store_dwordx2 v[6:7], v[18:19], off
	v_cvt_pk_fp8_f32 v2, v5, v9 op_sel:[0,0,1]
	v_ashrrev_i32_e32 v7, 31, v4
	v_mad_u64_u32 v[4:5], s[2:3], v4, s17, v[52:53]
	v_mov_b32_e32 v6, v5
	v_mad_u64_u32 v[6:7], s[2:3], v7, s17, v[6:7]
	v_cvt_pk_fp8_f32 v3, v29, v51 op_sel:[0,0,1]
	v_mov_b32_e32 v5, v6
	ds_read2_b32 v[6:7], v78 offset0:16 offset1:24
	ds_read2_b32 v[8:9], v78 offset0:49 offset1:57
	ds_read2_b32 v[18:19], v78 offset0:82 offset1:90
	ds_read2_b32 v[20:21], v78 offset0:115 offset1:123
	ds_read2_b32 v[28:29], v78 offset0:148 offset1:156
	ds_read2_b32 v[50:51], v78 offset0:181 offset1:189
	v_lshl_add_u64 v[4:5], v[4:5], 0, s[12:13]
	v_mov_b32_e32 v26, 0
	ds_read2_b32 v[54:55], v78 offset0:214 offset1:222
	ds_read2_b32 v[56:57], v78 offset0:247 offset1:255
	v_mov_b32_e32 v27, 0
	s_waitcnt lgkmcnt(6)
	v_cvt_pk_fp8_f32 v26, v6, v8
	s_waitcnt lgkmcnt(2)
	v_cvt_pk_fp8_f32 v27, v28, v50
	v_lshl_add_u64 v[4:5], v[4:5], 0, v[70:71]
	global_store_dwordx2 v[4:5], v[2:3], off
	v_add_u32_e32 v2, s37, v76
	v_ashrrev_i32_e32 v5, 31, v2
	v_mad_u64_u32 v[2:3], s[2:3], v2, s17, v[52:53]
	v_mov_b32_e32 v4, v3
	v_cvt_pk_fp8_f32 v26, v18, v20 op_sel:[0,0,1]
	s_waitcnt lgkmcnt(0)
	v_cvt_pk_fp8_f32 v27, v54, v56 op_sel:[0,0,1]
	v_mad_u64_u32 v[4:5], s[2:3], v5, s17, v[4:5]
	v_mov_b32_e32 v3, v4
	v_lshl_add_u64 v[2:3], v[2:3], 0, s[12:13]
	v_mov_b32_e32 v4, 0
	v_mov_b32_e32 v5, 0
	v_cvt_pk_fp8_f32 v4, v7, v9
	v_cvt_pk_fp8_f32 v5, v29, v51
	v_lshl_add_u64 v[2:3], v[2:3], 0, v[70:71]
	global_store_dwordx2 v[2:3], v[26:27], off
	v_add_u32_e32 v2, s37, v77
	v_ashrrev_i32_e32 v7, 31, v2
	v_mad_u64_u32 v[2:3], s[2:3], v2, s17, v[52:53]
	v_mov_b32_e32 v6, v3
	v_cvt_pk_fp8_f32 v4, v19, v21 op_sel:[0,0,1]
	v_cvt_pk_fp8_f32 v5, v55, v57 op_sel:[0,0,1]
	v_mad_u64_u32 v[6:7], s[2:3], v7, s17, v[6:7]
	v_mov_b32_e32 v3, v6
	v_lshl_add_u64 v[2:3], v[2:3], 0, s[12:13]
	v_lshl_add_u64 v[2:3], v[2:3], 0, v[70:71]
	global_store_dwordx2 v[2:3], v[4:5], off
	s_waitcnt lgkmcnt(0)
	s_waitcnt vmcnt(4)
	v_mov_b64_e32 v[64:65], v[12:13]
	v_mov_b64_e32 v[60:61], v[16:17]
	v_mov_b64_e32 v[56:57], v[24:25]
	v_mov_b64_e32 v[52:53], v[32:33]
	v_mov_b64_e32 v[26:27], v[34:35]
	v_mov_b64_e32 v[18:19], v[38:39]
	v_mov_b64_e32 v[6:7], v[42:43]
	v_mov_b64_e32 v[2:3], v[46:47]
	s_add_i32 s7, s7, s44
	s_andn2_b64 vcc, exec, s[24:25]
	v_mov_b64_e32 v[62:63], v[10:11]
	v_mov_b64_e32 v[58:59], v[14:15]
	v_mov_b64_e32 v[54:55], v[22:23]
	v_mov_b64_e32 v[50:51], v[30:31]
	v_mov_b64_e32 v[28:29], v[36:37]
	v_mov_b64_e32 v[20:21], v[40:41]
	v_mov_b64_e32 v[8:9], v[44:45]
	v_mov_b64_e32 v[4:5], v[48:49]
	s_mov_b64 s[18:19], s[38:39]
	s_mov_b64 s[14:15], s[22:23]
	s_mov_b32 s12, s49
	s_mov_b32 s17, s47
	s_mov_b32 s37, s48
	s_mov_b32 s16, s50
	s_cbranch_vccz .LBB0_126
.LBB0_104:
	s_add_i32 s46, s46, s8
	s_cmp_gt_i32 s46, 0xbfff
	s_cselect_b64 s[24:25], -1, 0
	s_and_b64 vcc, exec, s[24:25]
	s_mov_b32 s49, s12
	s_mov_b32 s50, s16
	s_cmp_eq_u64 s[18:19], 0
	s_cbranch_scc1 .Lmw_nogain
	s_ashr_i32 s13, s12, 31
	v_lshl_add_u64 v[92:93], s[12:13], 0, v[66:67]
	v_lshl_add_u64 v[92:93], v[92:93], 2, s[18:19]
	global_load_dword v94, v[92:93], off
	global_load_dword v95, v[92:93], off offset:32
	global_load_dword v96, v[92:93], off offset:64
	global_load_dword v97, v[92:93], off offset:96
	global_load_dword v98, v[92:93], off offset:128
	global_load_dword v99, v[92:93], off offset:160
	global_load_dword v100, v[92:93], off offset:192
	global_load_dword v101, v[92:93], off offset:224
.Lmw_nogain:
	s_cbranch_vccnz .Lmw_last
	s_mul_hi_i32 s2, s46, 0x2aaaaaab
	s_lshr_b32 s3, s2, 31
	s_ashr_i32 s2, s2, 8
	s_add_i32 s42, s2, s3
	s_mul_i32 s2, s42, 0xfffffa00
	s_add_i32 s13, s46, s2
	s_cmpk_gt_i32 s13, 0x3ff
	s_mov_b64 s[38:39], -1
	s_cbranch_scc0 .LBB0_107
	s_load_dwordx2 s[2:3], s[0:1], 0x100
	s_and_b32 s22, s13, 0x7fffffc0
	s_ashr_i32 s43, s42, 31
	s_add_i32 s49, s22, 0xfffffc00
	s_lshl_b64 s[22:23], s[42:43], 22
	s_waitcnt lgkmcnt(0)
	s_add_u32 s2, s2, s22
	s_addc_u32 s3, s3, s23
	s_and_b32 s40, s7, 0x7e0
	s_lshl_b64 s[22:23], s[42:43], 20
	s_add_u32 s22, s35, s22
	s_addc_u32 s23, s36, s23
	s_mov_b64 s[38:39], 0

; #define LAS __attribute__((address_space(3)))
; __device__ __forceinline__ void tr8_finish(const TrRegs& R, const TrP& p, LAS float* scr, int lane) {
;     const int nq = (lane & 7) * 4, kr = lane >> 3;
; #pragma unroll
;     for (int i = 0; i < 8; ++i) { const int kk = 8 * i + kr; float gs = p.scale; if (p.gain) gs *= p.gain[p.k0 + kk];
;         LAS float* d = scr + kk * 33 + nq; d[0] = R.v[i][0] * gs; d[1] = R.v[i][1] * gs; d[2] = R.v[i][2] * gs; d[3] = R.v[i][3] * gs; }
.LBB0_111:
	s_cmp_lg_u64 s[18:19], 0
	s_cselect_b64 s[40:41], -1, 0
	s_cmp_eq_u64 s[18:19], 0
	s_cbranch_scc1 .LBB0_122
	s_waitcnt vmcnt(14)
	v_mul_f32_e32 v72, s16, v94
	v_mul_f32_e32 v74, s16, v95
	v_pk_mul_f32 v[80:81], v[62:63], v[72:73] op_sel_hi:[1,0]
	v_pk_mul_f32 v[72:73], v[64:65], v[72:73] op_sel_hi:[1,0]
	ds_write2_b32 v79, v80, v81 offset1:1
	ds_write2_b32 v79, v72, v73 offset0:2 offset1:3
	v_mov_b64_e32 v[72:73], v[74:75]
	s_cbranch_execnz .LBB0_114
.LBB0_113:
	v_pk_mul_f32 v[62:63], v[62:63], s[16:17] op_sel_hi:[1,0]
	ds_write2_b32 v79, v62, v63 offset1:1
	v_pk_mul_f32 v[62:63], v[64:65], s[16:17] op_sel_hi:[1,0]
	v_mov_b32_e32 v74, s16
	ds_write2_b32 v79, v62, v63 offset0:2 offset1:3
.LBB0_114:
	v_mov_b32_e32 v73, v74
	v_pk_mul_f32 v[58:59], v[58:59], v[72:73]
	v_add_u32_e32 v62, 0x420, v79
	ds_write2_b32 v62, v58, v59 offset1:1
	v_pk_mul_f32 v[58:59], v[60:61], v[72:73]
	v_add_u32_e32 v60, 0x428, v79
	ds_write2_b32 v60, v58, v59 offset1:1
	v_cndmask_b32_e64 v58, 0, 1, s[40:41]
	v_cmp_ne_u32_e64 s[2:3], 1, v58
	s_andn2_b64 vcc, exec, s[40:41]
	v_add_u32_e32 v62, 0x840, v79
	v_add_u32_e32 v61, 0x848, v79
	s_cbranch_vccnz .LBB0_123
	s_ashr_i32 s13, s12, 31
	s_waitcnt vmcnt(12)
	v_mul_f32_e32 v58, s16, v96
	v_mul_f32_e32 v60, s16, v97
	v_pk_mul_f32 v[64:65], v[54:55], v[58:59] op_sel_hi:[1,0]
	v_pk_mul_f32 v[58:59], v[56:57], v[58:59] op_sel_hi:[1,0]
	ds_write2_b32 v62, v64, v65 offset1:1
	ds_write2_b32 v61, v58, v59 offset1:1
	v_mov_b64_e32 v[58:59], v[60:61]
	s_cbranch_execnz .LBB0_117

; #define LAS __attribute__((address_space(3)))
; __device__ __forceinline__ void tr8_finish(const TrRegs& R, const TrP& p, LAS float* scr, int lane) {
;     ...
;     for (int i = 0; i < 8; ++i) { const int kk = 8 * i + kr; float gs = p.scale; if (p.gain) gs *= p.gain[p.k0 + kk];
;         LAS float* d = scr + kk * 33 + nq; d[0] = R.v[i][0] * gs; d[1] = R.v[i][1] * gs; d[2] = R.v[i][2] * gs; d[3] = R.v[i][3] * gs; }
.LBB0_117:
	v_mov_b32_e32 v59, v60
	v_pk_mul_f32 v[50:51], v[50:51], v[58:59]
	v_add_u32_e32 v54, 0xc60, v79
	ds_write2_b32 v54, v50, v51 offset1:1
	v_pk_mul_f32 v[50:51], v[52:53], v[58:59]
	v_add_u32_e32 v52, 0xc68, v79
	s_and_b64 vcc, exec, s[2:3]
	v_add_u32_e32 v54, 0x1080, v79
	v_add_u32_e32 v53, 0x1088, v79
	ds_write2_b32 v52, v50, v51 offset1:1
	s_cbranch_vccnz .LBB0_124
	s_ashr_i32 s13, s12, 31
	s_waitcnt vmcnt(10)
	v_mul_f32_e32 v50, s16, v98
	v_mul_f32_e32 v52, s16, v99
	v_pk_mul_f32 v[56:57], v[26:27], v[50:51] op_sel_hi:[1,0]
	v_pk_mul_f32 v[50:51], v[28:29], v[50:51] op_sel_hi:[1,0]
	ds_write2_b32 v54, v56, v57 offset1:1
	ds_write2_b32 v53, v50, v51 offset1:1
	v_mov_b64_e32 v[50:51], v[52:53]
	s_cbranch_execnz .LBB0_120

; #define LAS __attribute__((address_space(3)))
; __device__ __forceinline__ void tr8_finish(const TrRegs& R, const TrP& p, LAS float* scr, int lane) {
;     ...
;     for (int i = 0; i < 8; ++i) { const int kk = 8 * i + kr; float gs = p.scale; if (p.gain) gs *= p.gain[p.k0 + kk];
;         LAS float* d = scr + kk * 33 + nq; d[0] = R.v[i][0] * gs; d[1] = R.v[i][1] * gs; d[2] = R.v[i][2] * gs; d[3] = R.v[i][3] * gs; }
.LBB0_120:
	v_mov_b32_e32 v51, v52
	v_pk_mul_f32 v[18:19], v[18:19], v[50:51]
	v_add_u32_e32 v26, 0x14a0, v79
	ds_write2_b32 v26, v18, v19 offset1:1
	v_pk_mul_f32 v[18:19], v[20:21], v[50:51]
	v_add_u32_e32 v20, 0x14a8, v79
	s_and_b64 vcc, exec, s[2:3]
	v_add_u32_e32 v26, 0x18c0, v79
	v_add_u32_e32 v21, 0x18c8, v79
	ds_write2_b32 v20, v18, v19 offset1:1
	s_cbranch_vccnz .LBB0_125
	s_ashr_i32 s13, s12, 31
	s_waitcnt vmcnt(8)
	v_mul_f32_e32 v18, s16, v100
	v_mul_f32_e32 v20, s16, v101
	v_pk_mul_f32 v[28:29], v[6:7], v[18:19] op_sel_hi:[1,0]
	v_pk_mul_f32 v[18:19], v[8:9], v[18:19] op_sel_hi:[1,0]
	ds_write2_b32 v26, v28, v29 offset1:1
	ds_write2_b32 v21, v18, v19 offset1:1
	v_mov_b64_e32 v[18:19], v[20:21]
	s_cbranch_execnz .LBB0_103
	s_branch .LBB0_102

; __device__ __forceinline__ void moe_weight_items(Frame& F, int layer, int gw, int NGW) {
;     ...
;     for (int it = gw; it < MOE_ITEMS; it += NGW) {
;         const int nx = it + NGW; TrP pn = pc; TrRegs rn;
;         if (nx < MOE_ITEMS) { pn = moe_item_params(layer, nx, WGU, WD); tr8_load(rn, pn, F.lane); }
;         tr8_finish(rc, pc, scr, F.lane);
;         if (nx < MOE_ITEMS) { pc = pn; rc = rn; }
;     }
.Lmw_last:
	s_waitcnt vmcnt(0)
	s_branch .LBB0_111
